# baseline (speedup 1.0000x reference)
.Lhold_done:
	s_cmp_lt_u32 s2, 0x100
	s_cbranch_scc1 .Lprio_done
	s_setprio 2

.Lmid_bar:
	s_setprio 0
	s_barrier
	s_cbranch_execz .Lgather_done
